# attention blocks: static priority raise for waves 0-3 instead of 4-7
# speedup vs baseline: 1.0047x; 1.0047x over previous
; #define SUB(n) if constexpr ((SUBMASK >> (n)) & 1)
; DEVI int obid() { int b = blockIdx.x; asm volatile("" : "+s"(b)); return b; }
; DEVI void phase_l4(const Params& p, int l, char* smem) {
;     ...
; #pragma nounroll
;     for (int rep = 0; rep < L4_ATT_REP; ++rep)
; #pragma nounroll
;     for (int it = 0; ; ++it) {
;         int u;
;         if (!spec) { u = obid() + it * gridDim.x; if (u >= nal + nac) break; }
;         else { if (it >= 2) break; u = (it == 0) ? obid() : (obid() < nac ? nal + obid() : (dbl ? obid() + L4NC : -1)); if (u < 0) break; }
;         if (u < nal) { SUB(4) {
;             const int bh = u >> 3, qb = u & 7, b = bh >> 3, h = bh & 7;
;             att::attn_body(Q + ((size_t)bh * KEYS + CL + qb * 256) * 192, Kb + (size_t)bh * KEYS * 192, Vb + (size_t)bh * KEYS * 128,
;                            ymix + (size_t)(b * SEQ + qb * 256) * DM + h * 128, KEYS, smem);
.LBB0_644:
	v_readfirstlane_b32 s4, v0
	s_nop 3
	s_lshr_b32 s4, s4, 8
	s_cmp_eq_u32 s4, 0
	s_cbranch_scc0 .Lattn_prio_skip
	s_setprio 1
